# waitcnt placement (strategy 1): MoE down-projection epilogues (both layers) no longer wait for the previous block's write-through stores before each conditional store block; on top of v55
# baseline (speedup 1.0000x reference)
.LBB0_1134:
	v_lshlrev_b32_e32 v98, 16, v142
	v_and_b32_e32 v99, 0xffff0000, v142
	v_lshlrev_b32_e32 v100, 16, v143
	v_and_b32_e32 v101, 0xffff0000, v143
	v_pk_add_f32 v[96:97], v[96:97], v[100:101]
	v_pk_add_f32 v[94:95], v[94:95], v[98:99]
	v_lshlrev_b32_e32 v98, 16, v144
	v_and_b32_e32 v99, 0xffff0000, v144
	v_lshlrev_b32_e32 v100, 16, v145
	v_and_b32_e32 v101, 0xffff0000, v145
	v_pk_add_f32 v[100:101], v[92:93], v[100:101]
	v_pk_add_f32 v[92:93], v[90:91], v[98:99]
	v_cvt_pk_bf16_f32 v90, v94, v95
	v_lshl_add_u64 v[94:95], s[2:3], 0, v[180:181]
	v_cvt_pk_bf16_f32 v91, v96, v97
	v_cvt_pk_bf16_f32 v92, v92, v93
	v_cvt_pk_bf16_f32 v93, v100, v101
	v_lshl_add_u64 v[94:95], v[166:167], 1, v[94:95]
	global_store_dwordx4 v[94:95], v[90:93], off sc1
	s_nop 1
	v_lshlrev_b32_e32 v90, 16, v138
	v_and_b32_e32 v91, 0xffff0000, v138
	v_lshlrev_b32_e32 v92, 16, v139
	v_and_b32_e32 v93, 0xffff0000, v139
	v_pk_add_f32 v[88:89], v[88:89], v[92:93]
	v_pk_add_f32 v[86:87], v[86:87], v[90:91]
	v_lshlrev_b32_e32 v90, 16, v140
	v_and_b32_e32 v91, 0xffff0000, v140
	v_lshlrev_b32_e32 v92, 16, v141
	v_and_b32_e32 v93, 0xffff0000, v141
	v_pk_add_f32 v[92:93], v[84:85], v[92:93]
	v_pk_add_f32 v[84:85], v[82:83], v[90:91]
	v_cvt_pk_bf16_f32 v82, v86, v87
	v_cvt_pk_bf16_f32 v83, v88, v89
	s_nop 0
	v_cvt_pk_bf16_f32 v84, v84, v85
	v_cvt_pk_bf16_f32 v85, v92, v93
	global_store_dwordx4 v[94:95], v[82:85], off offset:256 sc1
	s_or_b64 exec, exec, s[18:19]
	s_and_saveexec_b64 s[16:17], s[14:15]
	s_cbranch_execnz .LBB0_1138
	s_branch .LBB0_1139
.LBB0_1135:
	s_waitcnt vmcnt(0)
	s_or_b64 exec, exec, s[64:65]
	s_and_saveexec_b64 s[20:21], s[18:19]
	s_cbranch_execz .LBB0_1133
.LBB0_1136:
	v_lshlrev_b32_e32 v114, 16, v150
	v_and_b32_e32 v115, 0xffff0000, v150
	v_lshlrev_b32_e32 v116, 16, v151
	v_and_b32_e32 v117, 0xffff0000, v151
	v_pk_add_f32 v[112:113], v[112:113], v[116:117]
	v_pk_add_f32 v[110:111], v[110:111], v[114:115]
	v_lshlrev_b32_e32 v114, 16, v152
	v_and_b32_e32 v115, 0xffff0000, v152
	v_lshlrev_b32_e32 v116, 16, v153
	v_and_b32_e32 v117, 0xffff0000, v153
	v_pk_add_f32 v[116:117], v[108:109], v[116:117]
	v_pk_add_f32 v[108:109], v[106:107], v[114:115]
	v_cvt_pk_bf16_f32 v106, v110, v111
	v_lshl_add_u64 v[110:111], s[2:3], 0, v[182:183]
	v_cvt_pk_bf16_f32 v107, v112, v113
	v_cvt_pk_bf16_f32 v108, v108, v109
	v_cvt_pk_bf16_f32 v109, v116, v117
	v_lshl_add_u64 v[110:111], v[166:167], 1, v[110:111]
	global_store_dwordx4 v[110:111], v[106:109], off sc1
	s_nop 1
	v_lshlrev_b32_e32 v106, 16, v146
	v_and_b32_e32 v107, 0xffff0000, v146
	v_lshlrev_b32_e32 v108, 16, v147
	v_and_b32_e32 v109, 0xffff0000, v147
	v_pk_add_f32 v[104:105], v[104:105], v[108:109]
	v_pk_add_f32 v[102:103], v[102:103], v[106:107]
	v_lshlrev_b32_e32 v106, 16, v148
	v_and_b32_e32 v107, 0xffff0000, v148
	v_lshlrev_b32_e32 v108, 16, v149
	v_and_b32_e32 v109, 0xffff0000, v149
	v_pk_add_f32 v[108:109], v[100:101], v[108:109]
	v_pk_add_f32 v[100:101], v[98:99], v[106:107]
	v_cvt_pk_bf16_f32 v98, v102, v103
	v_cvt_pk_bf16_f32 v99, v104, v105
	s_nop 0
	v_cvt_pk_bf16_f32 v100, v100, v101
	v_cvt_pk_bf16_f32 v101, v108, v109
	global_store_dwordx4 v[110:111], v[98:101], off offset:256 sc1
	s_or_b64 exec, exec, s[20:21]
	s_and_saveexec_b64 s[18:19], s[16:17]
	s_cbranch_execnz .LBB0_1134

.LBB0_1138:
	v_lshlrev_b32_e32 v82, 16, v134
	v_and_b32_e32 v83, 0xffff0000, v134
	v_lshlrev_b32_e32 v84, 16, v135
	v_and_b32_e32 v85, 0xffff0000, v135
	v_pk_add_f32 v[80:81], v[80:81], v[84:85]
	v_pk_add_f32 v[78:79], v[78:79], v[82:83]
	v_lshlrev_b32_e32 v82, 16, v136
	v_and_b32_e32 v83, 0xffff0000, v136
	v_lshlrev_b32_e32 v84, 16, v137
	v_and_b32_e32 v85, 0xffff0000, v137
	v_pk_add_f32 v[84:85], v[76:77], v[84:85]
	v_pk_add_f32 v[76:77], v[74:75], v[82:83]
	v_cvt_pk_bf16_f32 v74, v78, v79
	v_lshl_add_u64 v[78:79], s[2:3], 0, v[178:179]
	v_cvt_pk_bf16_f32 v75, v80, v81
	v_cvt_pk_bf16_f32 v76, v76, v77
	v_cvt_pk_bf16_f32 v77, v84, v85
	v_lshl_add_u64 v[78:79], v[166:167], 1, v[78:79]
	global_store_dwordx4 v[78:79], v[74:77], off sc1
	s_nop 1
	v_lshlrev_b32_e32 v74, 16, v130
	v_and_b32_e32 v75, 0xffff0000, v130
	v_lshlrev_b32_e32 v76, 16, v131
	v_and_b32_e32 v77, 0xffff0000, v131
	v_pk_add_f32 v[64:65], v[64:65], v[76:77]
	v_pk_add_f32 v[62:63], v[62:63], v[74:75]
	v_lshlrev_b32_e32 v74, 16, v132
	v_and_b32_e32 v75, 0xffff0000, v132
	v_lshlrev_b32_e32 v76, 16, v133
	v_and_b32_e32 v77, 0xffff0000, v133
	v_pk_add_f32 v[76:77], v[60:61], v[76:77]
	v_pk_add_f32 v[60:61], v[58:59], v[74:75]
	v_cvt_pk_bf16_f32 v58, v62, v63
	v_cvt_pk_bf16_f32 v59, v64, v65
	s_nop 0
	v_cvt_pk_bf16_f32 v60, v60, v61
	v_cvt_pk_bf16_f32 v61, v76, v77
	global_store_dwordx4 v[78:79], v[58:61], off offset:256 sc1

.LBB0_1142:
	v_lshlrev_b32_e32 v34, 16, v78
	v_and_b32_e32 v35, 0xffff0000, v78
	v_lshlrev_b32_e32 v36, 16, v79
	v_and_b32_e32 v37, 0xffff0000, v79
	v_pk_add_f32 v[32:33], v[32:33], v[36:37]
	v_pk_add_f32 v[30:31], v[30:31], v[34:35]
	v_lshlrev_b32_e32 v34, 16, v80
	v_and_b32_e32 v35, 0xffff0000, v80
	v_lshlrev_b32_e32 v36, 16, v81
	v_and_b32_e32 v37, 0xffff0000, v81
	v_pk_add_f32 v[36:37], v[28:29], v[36:37]
	v_pk_add_f32 v[28:29], v[26:27], v[34:35]
	v_cvt_pk_bf16_f32 v26, v30, v31
	v_lshl_add_u64 v[30:31], s[2:3], 0, v[92:93]
	v_cvt_pk_bf16_f32 v27, v32, v33
	v_cvt_pk_bf16_f32 v28, v28, v29
	v_cvt_pk_bf16_f32 v29, v36, v37
	v_lshl_add_u64 v[30:31], v[166:167], 1, v[30:31]
	global_store_dwordx4 v[30:31], v[26:29], off sc1
	s_nop 1
	v_lshlrev_b32_e32 v26, 16, v74
	v_and_b32_e32 v27, 0xffff0000, v74
	v_lshlrev_b32_e32 v28, 16, v75
	v_and_b32_e32 v29, 0xffff0000, v75
	v_pk_add_f32 v[24:25], v[24:25], v[28:29]
	v_pk_add_f32 v[22:23], v[22:23], v[26:27]
	v_lshlrev_b32_e32 v26, 16, v76
	v_and_b32_e32 v27, 0xffff0000, v76
	v_lshlrev_b32_e32 v28, 16, v77
	v_and_b32_e32 v29, 0xffff0000, v77
	v_pk_add_f32 v[28:29], v[20:21], v[28:29]
	v_pk_add_f32 v[20:21], v[18:19], v[26:27]
	v_cvt_pk_bf16_f32 v18, v22, v23
	v_cvt_pk_bf16_f32 v19, v24, v25
	s_nop 0
	v_cvt_pk_bf16_f32 v20, v20, v21
	v_cvt_pk_bf16_f32 v21, v28, v29
	global_store_dwordx4 v[30:31], v[18:21], off offset:256 sc1
	s_or_b64 exec, exec, s[10:11]
	s_and_saveexec_b64 s[8:9], vcc
	s_cbranch_execnz .LBB0_1147

.LBB0_1144:
	s_waitcnt vmcnt(0)
	s_or_b64 exec, exec, s[14:15]
	s_and_saveexec_b64 s[12:13], s[10:11]
	s_cbranch_execz .LBB0_1141
.LBB0_1145:
	v_lshlrev_b32_e32 v50, 16, v86
	v_and_b32_e32 v51, 0xffff0000, v86
	v_lshlrev_b32_e32 v52, 16, v87
	v_and_b32_e32 v53, 0xffff0000, v87
	v_pk_add_f32 v[48:49], v[48:49], v[52:53]
	v_pk_add_f32 v[46:47], v[46:47], v[50:51]
	v_lshlrev_b32_e32 v50, 16, v88
	v_and_b32_e32 v51, 0xffff0000, v88
	v_lshlrev_b32_e32 v52, 16, v89
	v_and_b32_e32 v53, 0xffff0000, v89
	v_pk_add_f32 v[52:53], v[44:45], v[52:53]
	v_pk_add_f32 v[44:45], v[42:43], v[50:51]
	v_cvt_pk_bf16_f32 v42, v46, v47
	v_lshl_add_u64 v[46:47], s[2:3], 0, v[94:95]
	v_cvt_pk_bf16_f32 v43, v48, v49
	v_cvt_pk_bf16_f32 v44, v44, v45
	v_cvt_pk_bf16_f32 v45, v52, v53
	v_lshl_add_u64 v[46:47], v[166:167], 1, v[46:47]
	global_store_dwordx4 v[46:47], v[42:45], off sc1
	s_nop 1
	v_lshlrev_b32_e32 v42, 16, v82
	v_and_b32_e32 v43, 0xffff0000, v82
	v_lshlrev_b32_e32 v44, 16, v83
	v_and_b32_e32 v45, 0xffff0000, v83
	v_pk_add_f32 v[40:41], v[40:41], v[44:45]
	v_pk_add_f32 v[38:39], v[38:39], v[42:43]
	v_lshlrev_b32_e32 v42, 16, v84
	v_and_b32_e32 v43, 0xffff0000, v84
	v_lshlrev_b32_e32 v44, 16, v85
	v_and_b32_e32 v45, 0xffff0000, v85
	v_pk_add_f32 v[44:45], v[36:37], v[44:45]
	v_pk_add_f32 v[36:37], v[34:35], v[42:43]
	v_cvt_pk_bf16_f32 v34, v38, v39
	v_cvt_pk_bf16_f32 v35, v40, v41
	s_nop 0
	v_cvt_pk_bf16_f32 v36, v36, v37
	v_cvt_pk_bf16_f32 v37, v44, v45
	global_store_dwordx4 v[46:47], v[34:37], off offset:256 sc1
	s_or_b64 exec, exec, s[12:13]
	s_and_saveexec_b64 s[10:11], s[8:9]
	s_cbranch_execnz .LBB0_1142

.LBB0_1147:
	v_lshlrev_b32_e32 v18, 16, v62
	v_and_b32_e32 v19, 0xffff0000, v62
	v_lshlrev_b32_e32 v20, 16, v63
	v_and_b32_e32 v21, 0xffff0000, v63
	v_pk_add_f32 v[16:17], v[16:17], v[20:21]
	v_pk_add_f32 v[14:15], v[14:15], v[18:19]
	v_lshlrev_b32_e32 v18, 16, v64
	v_and_b32_e32 v19, 0xffff0000, v64
	v_lshlrev_b32_e32 v20, 16, v65
	v_and_b32_e32 v21, 0xffff0000, v65
	v_pk_add_f32 v[20:21], v[12:13], v[20:21]
	v_pk_add_f32 v[12:13], v[10:11], v[18:19]
	v_cvt_pk_bf16_f32 v10, v14, v15
	v_lshl_add_u64 v[14:15], s[2:3], 0, v[90:91]
	v_cvt_pk_bf16_f32 v11, v16, v17
	v_cvt_pk_bf16_f32 v12, v12, v13
	v_cvt_pk_bf16_f32 v13, v20, v21
	v_lshl_add_u64 v[14:15], v[166:167], 1, v[14:15]
	global_store_dwordx4 v[14:15], v[10:13], off sc1
	s_nop 1
	v_lshlrev_b32_e32 v10, 16, v58
	v_and_b32_e32 v11, 0xffff0000, v58
	v_lshlrev_b32_e32 v12, 16, v59
	v_and_b32_e32 v13, 0xffff0000, v59
	v_pk_add_f32 v[8:9], v[8:9], v[12:13]
	v_pk_add_f32 v[6:7], v[6:7], v[10:11]
	v_lshlrev_b32_e32 v10, 16, v60
	v_and_b32_e32 v11, 0xffff0000, v60
	v_lshlrev_b32_e32 v12, 16, v61
	v_and_b32_e32 v13, 0xffff0000, v61
	v_pk_add_f32 v[12:13], v[4:5], v[12:13]
	v_pk_add_f32 v[4:5], v[2:3], v[10:11]
	v_cvt_pk_bf16_f32 v2, v6, v7
	v_cvt_pk_bf16_f32 v3, v8, v9
	s_nop 0
	v_cvt_pk_bf16_f32 v4, v4, v5
	v_cvt_pk_bf16_f32 v5, v12, v13
	global_store_dwordx4 v[14:15], v[2:5], off offset:256 sc1
	s_or_b64 exec, exec, s[8:9]
	s_and_b64 vcc, exec, s[6:7]
	s_mov_b64 s[6:7], -1
	s_cbranch_vccnz .LBB0_1074

.LBB0_2181:
	v_lshlrev_b32_e32 v96, 16, v140
	v_and_b32_e32 v97, 0xffff0000, v140
	v_pk_add_f32 v[92:93], v[92:93], v[96:97]
	v_lshlrev_b32_e32 v96, 16, v142
	v_and_b32_e32 v97, 0xffff0000, v142
	v_readlane_b32 s36, v253, 46
	v_lshlrev_b32_e32 v98, 16, v141
	v_and_b32_e32 v99, 0xffff0000, v141
	v_pk_add_f32 v[88:89], v[88:89], v[96:97]
	v_lshlrev_b64 v[96:97], 12, v[176:177]
	v_readlane_b32 s48, v253, 58
	v_readlane_b32 s49, v253, 59
	v_pk_add_f32 v[94:95], v[94:95], v[98:99]
	v_lshlrev_b32_e32 v98, 16, v143
	v_and_b32_e32 v99, 0xffff0000, v143
	v_lshl_add_u64 v[96:97], s[48:49], 0, v[96:97]
	v_pk_add_f32 v[90:91], v[90:91], v[98:99]
	v_lshl_add_u64 v[96:97], v[162:163], 2, v[96:97]
	global_store_dwordx4 v[96:97], v[92:95], off nt
	global_store_dwordx4 v[96:97], v[88:91], off offset:16 nt
	v_readlane_b32 s37, v253, 47
	v_readlane_b32 s38, v253, 48
	v_lshlrev_b32_e32 v88, 16, v136
	v_and_b32_e32 v89, 0xffff0000, v136
	v_lshlrev_b32_e32 v90, 16, v137
	v_and_b32_e32 v91, 0xffff0000, v137
	v_pk_add_f32 v[86:87], v[86:87], v[90:91]
	v_pk_add_f32 v[84:85], v[84:85], v[88:89]
	v_lshlrev_b32_e32 v88, 16, v138
	v_and_b32_e32 v89, 0xffff0000, v138
	v_lshlrev_b32_e32 v90, 16, v139
	v_and_b32_e32 v91, 0xffff0000, v139
	v_readlane_b32 s39, v253, 49
	v_readlane_b32 s40, v253, 50
	v_readlane_b32 s41, v253, 51
	v_readlane_b32 s42, v253, 52
	v_readlane_b32 s43, v253, 53
	v_readlane_b32 s44, v253, 54
	v_readlane_b32 s45, v253, 55
	v_readlane_b32 s46, v253, 56
	v_readlane_b32 s47, v253, 57
	v_readlane_b32 s50, v253, 60
	v_readlane_b32 s51, v253, 61
	v_pk_add_f32 v[82:83], v[82:83], v[90:91]
	v_pk_add_f32 v[80:81], v[80:81], v[88:89]
	global_store_dwordx4 v[96:97], v[84:87], off offset:512 nt
	global_store_dwordx4 v[96:97], v[80:83], off offset:528 nt
	s_or_b64 exec, exec, s[14:15]
	s_and_saveexec_b64 s[12:13], s[10:11]
	s_cbranch_execnz .LBB0_2185
	s_branch .LBB0_2186
.LBB0_2182:
	s_waitcnt vmcnt(0)
	s_or_b64 exec, exec, s[58:59]
	s_and_saveexec_b64 s[16:17], s[14:15]
	s_cbranch_execz .LBB0_2180
.LBB0_2183:
	v_lshlrev_b32_e32 v112, 16, v148
	v_and_b32_e32 v113, 0xffff0000, v148
	v_pk_add_f32 v[108:109], v[108:109], v[112:113]
	v_lshlrev_b32_e32 v112, 16, v150
	v_and_b32_e32 v113, 0xffff0000, v150
	v_readlane_b32 s36, v253, 46
	v_lshlrev_b32_e32 v114, 16, v149
	v_and_b32_e32 v115, 0xffff0000, v149
	v_pk_add_f32 v[104:105], v[104:105], v[112:113]
	v_lshlrev_b64 v[112:113], 12, v[178:179]
	v_readlane_b32 s48, v253, 58
	v_readlane_b32 s49, v253, 59
	v_pk_add_f32 v[110:111], v[110:111], v[114:115]
	v_lshlrev_b32_e32 v114, 16, v151
	v_and_b32_e32 v115, 0xffff0000, v151
	v_lshl_add_u64 v[112:113], s[48:49], 0, v[112:113]
	v_pk_add_f32 v[106:107], v[106:107], v[114:115]
	v_lshl_add_u64 v[112:113], v[162:163], 2, v[112:113]
	global_store_dwordx4 v[112:113], v[108:111], off nt
	global_store_dwordx4 v[112:113], v[104:107], off offset:16 nt
	v_readlane_b32 s37, v253, 47
	v_readlane_b32 s38, v253, 48
	v_lshlrev_b32_e32 v104, 16, v144
	v_and_b32_e32 v105, 0xffff0000, v144
	v_lshlrev_b32_e32 v106, 16, v145
	v_and_b32_e32 v107, 0xffff0000, v145
	v_pk_add_f32 v[102:103], v[102:103], v[106:107]
	v_pk_add_f32 v[100:101], v[100:101], v[104:105]
	v_lshlrev_b32_e32 v104, 16, v146
	v_and_b32_e32 v105, 0xffff0000, v146
	v_lshlrev_b32_e32 v106, 16, v147
	v_and_b32_e32 v107, 0xffff0000, v147
	v_readlane_b32 s39, v253, 49
	v_readlane_b32 s40, v253, 50
	v_readlane_b32 s41, v253, 51
	v_readlane_b32 s42, v253, 52
	v_readlane_b32 s43, v253, 53
	v_readlane_b32 s44, v253, 54
	v_readlane_b32 s45, v253, 55
	v_readlane_b32 s46, v253, 56
	v_readlane_b32 s47, v253, 57
	v_readlane_b32 s50, v253, 60
	v_readlane_b32 s51, v253, 61
	v_pk_add_f32 v[98:99], v[98:99], v[106:107]
	v_pk_add_f32 v[96:97], v[96:97], v[104:105]
	global_store_dwordx4 v[112:113], v[100:103], off offset:512 nt
	global_store_dwordx4 v[112:113], v[96:99], off offset:528 nt
	s_or_b64 exec, exec, s[16:17]
	s_and_saveexec_b64 s[14:15], s[12:13]
	s_cbranch_execnz .LBB0_2181

.LBB0_2185:
	v_lshlrev_b32_e32 v80, 16, v132
	v_and_b32_e32 v81, 0xffff0000, v132
	v_pk_add_f32 v[76:77], v[76:77], v[80:81]
	v_lshlrev_b32_e32 v80, 16, v134
	v_and_b32_e32 v81, 0xffff0000, v134
	v_readlane_b32 s36, v253, 46
	v_lshlrev_b32_e32 v82, 16, v133
	v_and_b32_e32 v83, 0xffff0000, v133
	v_pk_add_f32 v[72:73], v[72:73], v[80:81]
	v_lshlrev_b64 v[80:81], 12, v[174:175]
	v_readlane_b32 s48, v253, 58
	v_readlane_b32 s49, v253, 59
	v_pk_add_f32 v[78:79], v[78:79], v[82:83]
	v_lshlrev_b32_e32 v82, 16, v135
	v_and_b32_e32 v83, 0xffff0000, v135
	v_lshl_add_u64 v[80:81], s[48:49], 0, v[80:81]
	v_pk_add_f32 v[74:75], v[74:75], v[82:83]
	v_lshl_add_u64 v[80:81], v[162:163], 2, v[80:81]
	global_store_dwordx4 v[80:81], v[76:79], off nt
	global_store_dwordx4 v[80:81], v[72:75], off offset:16 nt
	v_readlane_b32 s37, v253, 47
	v_readlane_b32 s38, v253, 48
	v_lshlrev_b32_e32 v72, 16, v128
	v_and_b32_e32 v73, 0xffff0000, v128
	v_lshlrev_b32_e32 v74, 16, v129
	v_and_b32_e32 v75, 0xffff0000, v129
	v_pk_add_f32 v[70:71], v[70:71], v[74:75]
	v_pk_add_f32 v[68:69], v[68:69], v[72:73]
	v_lshlrev_b32_e32 v72, 16, v130
	v_and_b32_e32 v73, 0xffff0000, v130
	v_lshlrev_b32_e32 v74, 16, v131
	v_and_b32_e32 v75, 0xffff0000, v131
	v_readlane_b32 s39, v253, 49
	v_readlane_b32 s40, v253, 50
	v_readlane_b32 s41, v253, 51
	v_readlane_b32 s42, v253, 52
	v_readlane_b32 s43, v253, 53
	v_readlane_b32 s44, v253, 54
	v_readlane_b32 s45, v253, 55
	v_readlane_b32 s46, v253, 56
	v_readlane_b32 s47, v253, 57
	v_readlane_b32 s50, v253, 60
	v_readlane_b32 s51, v253, 61
	v_pk_add_f32 v[66:67], v[66:67], v[74:75]
	v_pk_add_f32 v[64:65], v[64:65], v[72:73]
	global_store_dwordx4 v[80:81], v[68:71], off offset:512 nt
	global_store_dwordx4 v[80:81], v[64:67], off offset:528 nt

.LBB0_2189:
	v_lshlrev_b32_e32 v32, 16, v76
	v_and_b32_e32 v33, 0xffff0000, v76
	v_pk_add_f32 v[28:29], v[28:29], v[32:33]
	v_lshlrev_b32_e32 v32, 16, v78
	v_and_b32_e32 v33, 0xffff0000, v78
	v_readlane_b32 s36, v253, 46
	v_lshlrev_b32_e32 v34, 16, v77
	v_and_b32_e32 v35, 0xffff0000, v77
	v_pk_add_f32 v[24:25], v[24:25], v[32:33]
	v_lshlrev_b64 v[32:33], 12, v[166:167]
	v_readlane_b32 s48, v253, 58
	v_readlane_b32 s49, v253, 59
	v_pk_add_f32 v[30:31], v[30:31], v[34:35]
	v_lshlrev_b32_e32 v34, 16, v79
	v_and_b32_e32 v35, 0xffff0000, v79
	v_lshl_add_u64 v[32:33], s[48:49], 0, v[32:33]
	v_pk_add_f32 v[26:27], v[26:27], v[34:35]
	v_lshl_add_u64 v[32:33], v[162:163], 2, v[32:33]
	global_store_dwordx4 v[32:33], v[28:31], off nt
	global_store_dwordx4 v[32:33], v[24:27], off offset:16 nt
	v_readlane_b32 s37, v253, 47
	v_readlane_b32 s38, v253, 48
	v_lshlrev_b32_e32 v24, 16, v72
	v_and_b32_e32 v25, 0xffff0000, v72
	v_lshlrev_b32_e32 v26, 16, v73
	v_and_b32_e32 v27, 0xffff0000, v73
	v_pk_add_f32 v[22:23], v[22:23], v[26:27]
	v_pk_add_f32 v[20:21], v[20:21], v[24:25]
	v_lshlrev_b32_e32 v24, 16, v74
	v_and_b32_e32 v25, 0xffff0000, v74
	v_lshlrev_b32_e32 v26, 16, v75
	v_and_b32_e32 v27, 0xffff0000, v75
	v_readlane_b32 s39, v253, 49
	v_readlane_b32 s40, v253, 50
	v_readlane_b32 s41, v253, 51
	v_readlane_b32 s42, v253, 52
	v_readlane_b32 s43, v253, 53
	v_readlane_b32 s44, v253, 54
	v_readlane_b32 s45, v253, 55
	v_readlane_b32 s46, v253, 56
	v_readlane_b32 s47, v253, 57
	v_readlane_b32 s50, v253, 60
	v_readlane_b32 s51, v253, 61
	v_pk_add_f32 v[18:19], v[18:19], v[26:27]
	v_pk_add_f32 v[16:17], v[16:17], v[24:25]
	global_store_dwordx4 v[32:33], v[20:23], off offset:512 nt
	global_store_dwordx4 v[32:33], v[16:19], off offset:528 nt
	s_or_b64 exec, exec, s[6:7]
	s_and_saveexec_b64 s[4:5], vcc
	s_cbranch_execnz .LBB0_2194

.LBB0_2191:
	s_waitcnt vmcnt(0)
	s_or_b64 exec, exec, s[10:11]
	s_and_saveexec_b64 s[8:9], s[6:7]
	s_cbranch_execz .LBB0_2188
.LBB0_2192:
	v_lshlrev_b32_e32 v48, 16, v84
	v_and_b32_e32 v49, 0xffff0000, v84
	v_pk_add_f32 v[44:45], v[44:45], v[48:49]
	v_lshlrev_b32_e32 v48, 16, v86
	v_and_b32_e32 v49, 0xffff0000, v86
	v_readlane_b32 s36, v253, 46
	v_lshlrev_b32_e32 v50, 16, v85
	v_and_b32_e32 v51, 0xffff0000, v85
	v_pk_add_f32 v[40:41], v[40:41], v[48:49]
	v_lshlrev_b64 v[48:49], 12, v[168:169]
	v_readlane_b32 s48, v253, 58
	v_readlane_b32 s49, v253, 59
	v_pk_add_f32 v[46:47], v[46:47], v[50:51]
	v_lshlrev_b32_e32 v50, 16, v87
	v_and_b32_e32 v51, 0xffff0000, v87
	v_lshl_add_u64 v[48:49], s[48:49], 0, v[48:49]
	v_pk_add_f32 v[42:43], v[42:43], v[50:51]
	v_lshl_add_u64 v[48:49], v[162:163], 2, v[48:49]
	global_store_dwordx4 v[48:49], v[44:47], off nt
	global_store_dwordx4 v[48:49], v[40:43], off offset:16 nt
	v_readlane_b32 s37, v253, 47
	v_readlane_b32 s38, v253, 48
	v_lshlrev_b32_e32 v40, 16, v80
	v_and_b32_e32 v41, 0xffff0000, v80
	v_lshlrev_b32_e32 v42, 16, v81
	v_and_b32_e32 v43, 0xffff0000, v81
	v_pk_add_f32 v[38:39], v[38:39], v[42:43]
	v_pk_add_f32 v[36:37], v[36:37], v[40:41]
	v_lshlrev_b32_e32 v40, 16, v82
	v_and_b32_e32 v41, 0xffff0000, v82
	v_lshlrev_b32_e32 v42, 16, v83
	v_and_b32_e32 v43, 0xffff0000, v83
	v_readlane_b32 s39, v253, 49
	v_readlane_b32 s40, v253, 50
	v_readlane_b32 s41, v253, 51
	v_readlane_b32 s42, v253, 52
	v_readlane_b32 s43, v253, 53
	v_readlane_b32 s44, v253, 54
	v_readlane_b32 s45, v253, 55
	v_readlane_b32 s46, v253, 56
	v_readlane_b32 s47, v253, 57
	v_readlane_b32 s50, v253, 60
	v_readlane_b32 s51, v253, 61
	v_pk_add_f32 v[34:35], v[34:35], v[42:43]
	v_pk_add_f32 v[32:33], v[32:33], v[40:41]
	global_store_dwordx4 v[48:49], v[36:39], off offset:512 nt
	global_store_dwordx4 v[48:49], v[32:35], off offset:528 nt
	s_or_b64 exec, exec, s[8:9]
	s_and_saveexec_b64 s[6:7], s[4:5]
	s_cbranch_execnz .LBB0_2189

.LBB0_2194:
	v_lshlrev_b32_e32 v16, 16, v68
	v_and_b32_e32 v17, 0xffff0000, v68
	v_pk_add_f32 v[12:13], v[12:13], v[16:17]
	v_lshlrev_b32_e32 v16, 16, v70
	v_and_b32_e32 v17, 0xffff0000, v70
	v_readlane_b32 s36, v253, 46
	v_lshlrev_b32_e32 v18, 16, v69
	v_and_b32_e32 v19, 0xffff0000, v69
	v_pk_add_f32 v[8:9], v[8:9], v[16:17]
	v_lshlrev_b64 v[16:17], 12, v[164:165]
	v_readlane_b32 s48, v253, 58
	v_readlane_b32 s49, v253, 59
	v_pk_add_f32 v[14:15], v[14:15], v[18:19]
	v_lshlrev_b32_e32 v18, 16, v71
	v_and_b32_e32 v19, 0xffff0000, v71
	v_lshl_add_u64 v[16:17], s[48:49], 0, v[16:17]
	v_pk_add_f32 v[10:11], v[10:11], v[18:19]
	v_lshl_add_u64 v[16:17], v[162:163], 2, v[16:17]
	global_store_dwordx4 v[16:17], v[12:15], off nt
	global_store_dwordx4 v[16:17], v[8:11], off offset:16 nt
	v_readlane_b32 s37, v253, 47
	v_readlane_b32 s38, v253, 48
	v_lshlrev_b32_e32 v8, 16, v64
	v_and_b32_e32 v9, 0xffff0000, v64
	v_lshlrev_b32_e32 v10, 16, v65
	v_and_b32_e32 v11, 0xffff0000, v65
	v_pk_add_f32 v[6:7], v[6:7], v[10:11]
	v_pk_add_f32 v[4:5], v[4:5], v[8:9]
	v_lshlrev_b32_e32 v8, 16, v66
	v_and_b32_e32 v9, 0xffff0000, v66
	v_lshlrev_b32_e32 v10, 16, v67
	v_and_b32_e32 v11, 0xffff0000, v67
	v_readlane_b32 s39, v253, 49
	v_readlane_b32 s40, v253, 50
	v_readlane_b32 s41, v253, 51
	v_readlane_b32 s42, v253, 52
	v_readlane_b32 s43, v253, 53
	v_readlane_b32 s44, v253, 54
	v_readlane_b32 s45, v253, 55
	v_readlane_b32 s46, v253, 56
	v_readlane_b32 s47, v253, 57
	v_readlane_b32 s50, v253, 60
	v_readlane_b32 s51, v253, 61
	v_pk_add_f32 v[2:3], v[2:3], v[10:11]
	v_pk_add_f32 v[0:1], v[0:1], v[8:9]
	global_store_dwordx4 v[16:17], v[4:7], off offset:512 nt
	global_store_dwordx4 v[16:17], v[0:3], off offset:528 nt
	s_or_b64 exec, exec, s[4:5]
	s_and_b64 vcc, exec, s[2:3]
	s_mov_b64 s[2:3], -1
	s_cbranch_vccnz .LBB0_2121
